# grid barrier release read off the cross-XCD arrival counter (TOP >= (gen+1)*nx) instead of the generation word bumped after the last arrival returns: one atomic round trip less on the release path
# baseline (speedup 1.0000x reference)
; __device__ __forceinline__ unsigned xb_ld(unsigned* p)              { return __hip_atomic_load(p, __ATOMIC_RELAXED, __HIP_MEMORY_SCOPE_AGENT); }
; __device__ __forceinline__ unsigned xb_add(unsigned* p, unsigned v) { return __hip_atomic_fetch_add(p, v, __ATOMIC_RELAXED, __HIP_MEMORY_SCOPE_AGENT); }
; #define XB_SPIN(cond, bar) do { unsigned _sp = 0; while (cond) { __builtin_amdgcn_s_sleep(1); \
;     if ((++_sp & 255u) == 0u) { if (xb_ld(&(bar)[XB_TMO])) break; if (_sp > XB_SPIN_CAP) { atomicAdd(&(bar)[XB_TMO], 1u); break; } } } } while (0)
; __device__ __forceinline__ void xcd_barrier(const XcdBarrier& b) {
;     ...
;         const unsigned old = xb_add(&bar[XB_XSUB(b.x)], 1u);
;         const unsigned gen = old / nloc;
;         if (old + 1u == (gen + 1u) * nloc) {
;             __builtin_amdgcn_fence(__ATOMIC_RELEASE, "agent");
;             asm volatile("s_waitcnt vmcnt(0)" ::: "memory");
;             const unsigned og = xb_add(&bar[XB_TOP], 1u);
;             const unsigned tg = og / nx;
;             if (og + 1u == (tg + 1u) * nx) xb_add(&bar[XB_TOPGEN], 1u);
;             else XB_SPIN(xb_ld(&bar[XB_TOPGEN]) == tg, bar);
;             __builtin_amdgcn_fence(__ATOMIC_ACQUIRE, "agent");
;             xb_add(&bar[XB_XGEN(b.x)], 1u);
;             asm volatile("s_waitcnt vmcnt(0)" ::: "memory");
;         } else {
;             XB_SPIN(xb_ld(&bar[XB_XGEN(b.x)]) == gen, bar);
.LBB0_455:
	v_readlane_b32 s4, v254, 17
	v_readlane_b32 s5, v254, 18
	v_cvt_f32_u32_e32 v1, v4
	v_sub_u32_e32 v6, 0, v4
	v_rcp_iflag_f32_e32 v1, v1
	s_nop 1
	global_atomic_add v5, v3, v244, s[4:5] sc0
	v_mul_f32_e32 v1, 0x4f7ffffe, v1
	v_cvt_u32_f32_e32 v1, v1
	v_mul_lo_u32 v6, v6, v1
	v_mul_hi_u32 v6, v1, v6
	v_add_u32_e32 v1, v1, v6
	s_waitcnt vmcnt(0)
	v_mul_hi_u32 v1, v5, v1
	v_mul_lo_u32 v6, v1, v4
	v_sub_u32_e32 v6, v5, v6
	v_add_u32_e32 v7, 1, v1
	v_cmp_ge_u32_e32 vcc, v6, v4
	v_add_u32_e32 v5, 1, v5
	s_nop 0
	v_cndmask_b32_e32 v1, v1, v7, vcc
	v_sub_u32_e32 v7, v6, v4
	v_cndmask_b32_e32 v6, v6, v7, vcc
	v_add_u32_e32 v7, 1, v1
	v_cmp_ge_u32_e32 vcc, v6, v4
	s_nop 1
	v_cndmask_b32_e32 v1, v1, v7, vcc
	v_mul_lo_u32 v6, v4, v1
	v_add_u32_e32 v4, v6, v4
	v_cmp_ne_u32_e32 vcc, v5, v4
	s_and_saveexec_b64 s[4:5], vcc
	s_xor_b64 s[44:45], exec, s[4:5]
	s_cbranch_execz .LBB0_469
	v_readlane_b32 s4, v254, 21
	v_readlane_b32 s5, v254, 22
	s_waitcnt lgkmcnt(0)
	v_mad_u32_u24 v7, v1, v2, v2
	s_nop 3
	global_load_dword v2, v3, s[4:5] sc1
	s_waitcnt vmcnt(0)
	v_cmp_lt_u32_e32 vcc, v2, v7
	s_and_saveexec_b64 s[48:49], vcc
	s_cbranch_execz .LBB0_468
	s_mov_b32 s18, 1
	s_mov_b64 s[4:5], 0
	s_branch .LBB0_459

; __device__ __forceinline__ unsigned xb_ld(unsigned* p)              { return __hip_atomic_load(p, __ATOMIC_RELAXED, __HIP_MEMORY_SCOPE_AGENT); }
; #define XB_SPIN(cond, bar) do { unsigned _sp = 0; while (cond) { __builtin_amdgcn_s_sleep(1); \
;     if ((++_sp & 255u) == 0u) { if (xb_ld(&(bar)[XB_TMO])) break; if (_sp > XB_SPIN_CAP) { atomicAdd(&(bar)[XB_TMO], 1u); break; } } } } while (0)
; __device__ __forceinline__ void xcd_barrier(const XcdBarrier& b) {
;     ...
;             XB_SPIN(xb_ld(&bar[XB_XGEN(b.x)]) == gen, bar);
.LBB0_463:
	v_readlane_b32 s6, v254, 21
	v_readlane_b32 s7, v254, 22
	s_add_i32 s18, s18, 1
	s_mov_b64 s[8:9], -1
	s_nop 2
	global_load_dword v2, v3, s[6:7] sc1
	s_waitcnt vmcnt(0)
	v_cmp_ge_u32_e32 vcc, v2, v7
	s_orn2_b64 s[6:7], vcc, exec
	s_branch .LBB0_458

; __device__ __forceinline__ unsigned xb_ld(unsigned* p)              { return __hip_atomic_load(p, __ATOMIC_RELAXED, __HIP_MEMORY_SCOPE_AGENT); }
; __device__ __forceinline__ unsigned xb_add(unsigned* p, unsigned v) { return __hip_atomic_fetch_add(p, v, __ATOMIC_RELAXED, __HIP_MEMORY_SCOPE_AGENT); }
; #define XB_SPIN(cond, bar) do { unsigned _sp = 0; while (cond) { __builtin_amdgcn_s_sleep(1); \
;     if ((++_sp & 255u) == 0u) { if (xb_ld(&(bar)[XB_TMO])) break; if (_sp > XB_SPIN_CAP) { atomicAdd(&(bar)[XB_TMO], 1u); break; } } } } while (0)
; __device__ __forceinline__ void xcd_barrier(const XcdBarrier& b) {
;     ...
;             const unsigned og = xb_add(&bar[XB_TOP], 1u);
;             const unsigned tg = og / nx;
;             if (og + 1u == (tg + 1u) * nx) xb_add(&bar[XB_TOPGEN], 1u);
;             else XB_SPIN(xb_ld(&bar[XB_TOPGEN]) == tg, bar);
.LBB0_472:
	s_or_b64 exec, exec, s[6:7]
	s_waitcnt vmcnt(0)
	v_readfirstlane_b32 s4, v4
	v_sub_u32_e32 v5, 0, v2
	v_readlane_b32 s6, v254, 23
	v_add_u32_e32 v4, s4, v1
	v_cvt_f32_u32_e32 v1, v2
	v_readlane_b32 s7, v254, 24
	s_mov_b64 s[4:5], -1
	v_rcp_iflag_f32_e32 v1, v1
	s_nop 0
	v_mul_f32_e32 v1, 0x4f7ffffe, v1
	v_cvt_u32_f32_e32 v1, v1
	v_mul_lo_u32 v5, v5, v1
	v_mul_hi_u32 v5, v1, v5
	v_add_u32_e32 v1, v1, v5
	v_mul_hi_u32 v1, v4, v1
	v_mul_lo_u32 v5, v1, v2
	v_sub_u32_e32 v5, v4, v5
	v_cmp_ge_u32_e32 vcc, v5, v2
	v_add_u32_e32 v6, 1, v1
	v_add_u32_e32 v4, 1, v4
	v_cndmask_b32_e32 v1, v1, v6, vcc
	v_sub_u32_e32 v6, v5, v2
	v_cndmask_b32_e32 v5, v5, v6, vcc
	v_cmp_ge_u32_e32 vcc, v5, v2
	v_add_u32_e32 v5, 1, v1
	s_nop 0
	v_cndmask_b32_e32 v1, v1, v5, vcc
	v_mul_lo_u32 v5, v2, v1
	v_add_u32_e32 v2, v5, v2
	v_cmp_ne_u32_e32 vcc, v4, v2
	v_mov_b64_e32 v[4:5], s[6:7]
	s_and_saveexec_b64 s[44:45], vcc
	s_cbranch_execz .LBB0_484
	v_mov_b32_e32 v7, v2
	v_readlane_b32 s4, v254, 21
	v_readlane_b32 s5, v254, 22
	s_nop 4
	global_load_dword v2, v3, s[4:5] sc1
	s_mov_b64 s[4:5], 0
	s_waitcnt vmcnt(0)
	v_cmp_lt_u32_e32 vcc, v2, v7
	s_and_saveexec_b64 s[48:49], vcc
	s_cbranch_execz .LBB0_483
	s_mov_b32 s18, 1
	s_branch .LBB0_476

; __device__ __forceinline__ unsigned xb_ld(unsigned* p)              { return __hip_atomic_load(p, __ATOMIC_RELAXED, __HIP_MEMORY_SCOPE_AGENT); }
; __device__ __forceinline__ unsigned xb_add(unsigned* p, unsigned v) { return __hip_atomic_fetch_add(p, v, __ATOMIC_RELAXED, __HIP_MEMORY_SCOPE_AGENT); }
; #define XB_SPIN(cond, bar) do { unsigned _sp = 0; while (cond) { __builtin_amdgcn_s_sleep(1); \
;     if ((++_sp & 255u) == 0u) { if (xb_ld(&(bar)[XB_TMO])) break; if (_sp > XB_SPIN_CAP) { atomicAdd(&(bar)[XB_TMO], 1u); break; } } } } while (0)
; __device__ __forceinline__ void xcd_barrier(const XcdBarrier& b) {
;     ...
;         const unsigned old = xb_add(&bar[XB_XSUB(b.x)], 1u);
;         const unsigned gen = old / nloc;
;         if (old + 1u == (gen + 1u) * nloc) {
;             __builtin_amdgcn_fence(__ATOMIC_RELEASE, "agent");
;             asm volatile("s_waitcnt vmcnt(0)" ::: "memory");
;             const unsigned og = xb_add(&bar[XB_TOP], 1u);
;             const unsigned tg = og / nx;
;             if (og + 1u == (tg + 1u) * nx) xb_add(&bar[XB_TOPGEN], 1u);
;             else XB_SPIN(xb_ld(&bar[XB_TOPGEN]) == tg, bar);
;             __builtin_amdgcn_fence(__ATOMIC_ACQUIRE, "agent");
;             xb_add(&bar[XB_XGEN(b.x)], 1u);
;             asm volatile("s_waitcnt vmcnt(0)" ::: "memory");
;         } else {
;             XB_SPIN(xb_ld(&bar[XB_XGEN(b.x)]) == gen, bar);
.LBB0_548:
	v_readlane_b32 s4, v254, 17
	v_readlane_b32 s5, v254, 18
	v_cvt_f32_u32_e32 v1, v4
	v_sub_u32_e32 v6, 0, v4
	v_rcp_iflag_f32_e32 v1, v1
	s_nop 1
	global_atomic_add v5, v3, v244, s[4:5] sc0
	v_mul_f32_e32 v1, 0x4f7ffffe, v1
	v_cvt_u32_f32_e32 v1, v1
	v_mul_lo_u32 v6, v6, v1
	v_mul_hi_u32 v6, v1, v6
	v_add_u32_e32 v1, v1, v6
	s_waitcnt vmcnt(0)
	v_mul_hi_u32 v1, v5, v1
	v_mul_lo_u32 v6, v1, v4
	v_sub_u32_e32 v6, v5, v6
	v_add_u32_e32 v7, 1, v1
	v_cmp_ge_u32_e32 vcc, v6, v4
	v_add_u32_e32 v5, 1, v5
	s_nop 0
	v_cndmask_b32_e32 v1, v1, v7, vcc
	v_sub_u32_e32 v7, v6, v4
	v_cndmask_b32_e32 v6, v6, v7, vcc
	v_add_u32_e32 v7, 1, v1
	v_cmp_ge_u32_e32 vcc, v6, v4
	s_nop 1
	v_cndmask_b32_e32 v1, v1, v7, vcc
	v_mul_lo_u32 v6, v4, v1
	v_add_u32_e32 v4, v6, v4
	v_cmp_ne_u32_e32 vcc, v5, v4
	s_and_saveexec_b64 s[4:5], vcc
	s_xor_b64 s[40:41], exec, s[4:5]
	s_cbranch_execz .LBB0_562
	v_readlane_b32 s4, v254, 21
	v_readlane_b32 s5, v254, 22
	s_waitcnt lgkmcnt(0)
	v_mad_u32_u24 v7, v1, v2, v2
	s_nop 3
	global_load_dword v2, v3, s[4:5] sc1
	s_waitcnt vmcnt(0)
	v_cmp_lt_u32_e32 vcc, v2, v7
	s_and_saveexec_b64 s[42:43], vcc
	s_cbranch_execz .LBB0_561
	s_mov_b32 s18, 1
	s_mov_b64 s[4:5], 0
	s_branch .LBB0_552

; __device__ __forceinline__ unsigned xb_ld(unsigned* p)              { return __hip_atomic_load(p, __ATOMIC_RELAXED, __HIP_MEMORY_SCOPE_AGENT); }
; __device__ __forceinline__ unsigned xb_add(unsigned* p, unsigned v) { return __hip_atomic_fetch_add(p, v, __ATOMIC_RELAXED, __HIP_MEMORY_SCOPE_AGENT); }
; #define XB_SPIN(cond, bar) do { unsigned _sp = 0; while (cond) { __builtin_amdgcn_s_sleep(1); \
;     if ((++_sp & 255u) == 0u) { if (xb_ld(&(bar)[XB_TMO])) break; if (_sp > XB_SPIN_CAP) { atomicAdd(&(bar)[XB_TMO], 1u); break; } } } } while (0)
; __device__ __forceinline__ void xcd_barrier(const XcdBarrier& b) {
;     ...
;             const unsigned og = xb_add(&bar[XB_TOP], 1u);
;             const unsigned tg = og / nx;
;             if (og + 1u == (tg + 1u) * nx) xb_add(&bar[XB_TOPGEN], 1u);
;             else XB_SPIN(xb_ld(&bar[XB_TOPGEN]) == tg, bar);
.LBB0_565:
	s_or_b64 exec, exec, s[6:7]
	s_waitcnt vmcnt(0)
	v_readfirstlane_b32 s4, v4
	v_sub_u32_e32 v5, 0, v2
	v_readlane_b32 s6, v254, 23
	v_add_u32_e32 v4, s4, v1
	v_cvt_f32_u32_e32 v1, v2
	v_readlane_b32 s7, v254, 24
	s_mov_b64 s[4:5], -1
	v_rcp_iflag_f32_e32 v1, v1
	s_nop 0
	v_mul_f32_e32 v1, 0x4f7ffffe, v1
	v_cvt_u32_f32_e32 v1, v1
	v_mul_lo_u32 v5, v5, v1
	v_mul_hi_u32 v5, v1, v5
	v_add_u32_e32 v1, v1, v5
	v_mul_hi_u32 v1, v4, v1
	v_mul_lo_u32 v5, v1, v2
	v_sub_u32_e32 v5, v4, v5
	v_cmp_ge_u32_e32 vcc, v5, v2
	v_add_u32_e32 v6, 1, v1
	v_add_u32_e32 v4, 1, v4
	v_cndmask_b32_e32 v1, v1, v6, vcc
	v_sub_u32_e32 v6, v5, v2
	v_cndmask_b32_e32 v5, v5, v6, vcc
	v_cmp_ge_u32_e32 vcc, v5, v2
	v_add_u32_e32 v5, 1, v1
	s_nop 0
	v_cndmask_b32_e32 v1, v1, v5, vcc
	v_mul_lo_u32 v5, v2, v1
	v_add_u32_e32 v2, v5, v2
	v_cmp_ne_u32_e32 vcc, v4, v2
	v_mov_b64_e32 v[4:5], s[6:7]
	s_and_saveexec_b64 s[40:41], vcc
	s_cbranch_execz .LBB0_577
	v_mov_b32_e32 v7, v2
	v_readlane_b32 s4, v254, 21
	v_readlane_b32 s5, v254, 22
	s_nop 4
	global_load_dword v2, v3, s[4:5] sc1
	s_mov_b64 s[4:5], 0
	s_waitcnt vmcnt(0)
	v_cmp_lt_u32_e32 vcc, v2, v7
	s_and_saveexec_b64 s[42:43], vcc
	s_cbranch_execz .LBB0_576
	s_mov_b32 s18, 1
	s_branch .LBB0_569

; __device__ __forceinline__ unsigned xb_ld(unsigned* p)              { return __hip_atomic_load(p, __ATOMIC_RELAXED, __HIP_MEMORY_SCOPE_AGENT); }
; __device__ __forceinline__ unsigned xb_add(unsigned* p, unsigned v) { return __hip_atomic_fetch_add(p, v, __ATOMIC_RELAXED, __HIP_MEMORY_SCOPE_AGENT); }
; #define XB_SPIN(cond, bar) do { unsigned _sp = 0; while (cond) { __builtin_amdgcn_s_sleep(1); \
;     if ((++_sp & 255u) == 0u) { if (xb_ld(&(bar)[XB_TMO])) break; if (_sp > XB_SPIN_CAP) { atomicAdd(&(bar)[XB_TMO], 1u); break; } } } } while (0)
; __device__ __forceinline__ void xcd_barrier(const XcdBarrier& b) {
;     ...
;         const unsigned old = xb_add(&bar[XB_XSUB(b.x)], 1u);
;         const unsigned gen = old / nloc;
;         if (old + 1u == (gen + 1u) * nloc) {
;             __builtin_amdgcn_fence(__ATOMIC_RELEASE, "agent");
;             asm volatile("s_waitcnt vmcnt(0)" ::: "memory");
;             const unsigned og = xb_add(&bar[XB_TOP], 1u);
;             const unsigned tg = og / nx;
;             if (og + 1u == (tg + 1u) * nx) xb_add(&bar[XB_TOPGEN], 1u);
;             else XB_SPIN(xb_ld(&bar[XB_TOPGEN]) == tg, bar);
;             __builtin_amdgcn_fence(__ATOMIC_ACQUIRE, "agent");
;             xb_add(&bar[XB_XGEN(b.x)], 1u);
;             asm volatile("s_waitcnt vmcnt(0)" ::: "memory");
;         } else {
;             XB_SPIN(xb_ld(&bar[XB_XGEN(b.x)]) == gen, bar);
.LBB0_1538:
	v_readlane_b32 s4, v254, 17
	v_readlane_b32 s5, v254, 18
	v_cvt_f32_u32_e32 v1, v4
	v_sub_u32_e32 v6, 0, v4
	v_rcp_iflag_f32_e32 v1, v1
	s_nop 1
	global_atomic_add v5, v3, v244, s[4:5] sc0
	v_mul_f32_e32 v1, 0x4f7ffffe, v1
	v_cvt_u32_f32_e32 v1, v1
	v_mul_lo_u32 v6, v6, v1
	v_mul_hi_u32 v6, v1, v6
	v_add_u32_e32 v1, v1, v6
	s_waitcnt vmcnt(0)
	v_mul_hi_u32 v1, v5, v1
	v_mul_lo_u32 v6, v1, v4
	v_sub_u32_e32 v6, v5, v6
	v_add_u32_e32 v7, 1, v1
	v_cmp_ge_u32_e32 vcc, v6, v4
	v_add_u32_e32 v5, 1, v5
	s_nop 0
	v_cndmask_b32_e32 v1, v1, v7, vcc
	v_sub_u32_e32 v7, v6, v4
	v_cndmask_b32_e32 v6, v6, v7, vcc
	v_add_u32_e32 v7, 1, v1
	v_cmp_ge_u32_e32 vcc, v6, v4
	s_nop 1
	v_cndmask_b32_e32 v1, v1, v7, vcc
	v_mul_lo_u32 v6, v4, v1
	v_add_u32_e32 v4, v6, v4
	v_cmp_ne_u32_e32 vcc, v5, v4
	s_and_saveexec_b64 s[4:5], vcc
	s_xor_b64 s[40:41], exec, s[4:5]
	s_cbranch_execz .LBB0_1552
	v_readlane_b32 s4, v254, 21
	v_readlane_b32 s5, v254, 22
	s_waitcnt lgkmcnt(0)
	v_mad_u32_u24 v7, v1, v2, v2
	s_nop 3
	global_load_dword v2, v3, s[4:5] sc1
	s_waitcnt vmcnt(0)
	v_cmp_lt_u32_e32 vcc, v2, v7
	s_and_saveexec_b64 s[42:43], vcc
	s_cbranch_execz .LBB0_1551
	s_mov_b32 s17, 1
	s_mov_b64 s[4:5], 0
	s_branch .LBB0_1542

; __device__ __forceinline__ unsigned xb_ld(unsigned* p)              { return __hip_atomic_load(p, __ATOMIC_RELAXED, __HIP_MEMORY_SCOPE_AGENT); }
; #define XB_SPIN(cond, bar) do { unsigned _sp = 0; while (cond) { __builtin_amdgcn_s_sleep(1); \
;     if ((++_sp & 255u) == 0u) { if (xb_ld(&(bar)[XB_TMO])) break; if (_sp > XB_SPIN_CAP) { atomicAdd(&(bar)[XB_TMO], 1u); break; } } } } while (0)
; __device__ __forceinline__ void xcd_barrier(const XcdBarrier& b) {
;     ...
;             XB_SPIN(xb_ld(&bar[XB_XGEN(b.x)]) == gen, bar);
.LBB0_1546:
	v_readlane_b32 s6, v254, 21
	v_readlane_b32 s7, v254, 22
	s_add_i32 s17, s17, 1
	s_mov_b64 s[8:9], -1
	s_nop 2
	global_load_dword v2, v3, s[6:7] sc1
	s_waitcnt vmcnt(0)
	v_cmp_ge_u32_e32 vcc, v2, v7
	s_orn2_b64 s[6:7], vcc, exec
	s_branch .LBB0_1541

; __device__ __forceinline__ unsigned xb_ld(unsigned* p)              { return __hip_atomic_load(p, __ATOMIC_RELAXED, __HIP_MEMORY_SCOPE_AGENT); }
; __device__ __forceinline__ unsigned xb_add(unsigned* p, unsigned v) { return __hip_atomic_fetch_add(p, v, __ATOMIC_RELAXED, __HIP_MEMORY_SCOPE_AGENT); }
; #define XB_SPIN(cond, bar) do { unsigned _sp = 0; while (cond) { __builtin_amdgcn_s_sleep(1); \
;     if ((++_sp & 255u) == 0u) { if (xb_ld(&(bar)[XB_TMO])) break; if (_sp > XB_SPIN_CAP) { atomicAdd(&(bar)[XB_TMO], 1u); break; } } } } while (0)
; __device__ __forceinline__ void xcd_barrier(const XcdBarrier& b) {
;     ...
;             const unsigned og = xb_add(&bar[XB_TOP], 1u);
;             const unsigned tg = og / nx;
;             if (og + 1u == (tg + 1u) * nx) xb_add(&bar[XB_TOPGEN], 1u);
;             else XB_SPIN(xb_ld(&bar[XB_TOPGEN]) == tg, bar);
.LBB0_1555:
	s_or_b64 exec, exec, s[6:7]
	s_waitcnt vmcnt(0)
	v_readfirstlane_b32 s4, v4
	v_sub_u32_e32 v5, 0, v2
	v_readlane_b32 s6, v254, 23
	v_add_u32_e32 v4, s4, v1
	v_cvt_f32_u32_e32 v1, v2
	v_readlane_b32 s7, v254, 24
	s_mov_b64 s[4:5], -1
	v_rcp_iflag_f32_e32 v1, v1
	s_nop 0
	v_mul_f32_e32 v1, 0x4f7ffffe, v1
	v_cvt_u32_f32_e32 v1, v1
	v_mul_lo_u32 v5, v5, v1
	v_mul_hi_u32 v5, v1, v5
	v_add_u32_e32 v1, v1, v5
	v_mul_hi_u32 v1, v4, v1
	v_mul_lo_u32 v5, v1, v2
	v_sub_u32_e32 v5, v4, v5
	v_cmp_ge_u32_e32 vcc, v5, v2
	v_add_u32_e32 v6, 1, v1
	v_add_u32_e32 v4, 1, v4
	v_cndmask_b32_e32 v1, v1, v6, vcc
	v_sub_u32_e32 v6, v5, v2
	v_cndmask_b32_e32 v5, v5, v6, vcc
	v_cmp_ge_u32_e32 vcc, v5, v2
	v_add_u32_e32 v5, 1, v1
	s_nop 0
	v_cndmask_b32_e32 v1, v1, v5, vcc
	v_mul_lo_u32 v5, v2, v1
	v_add_u32_e32 v2, v5, v2
	v_cmp_ne_u32_e32 vcc, v4, v2
	v_mov_b64_e32 v[4:5], s[6:7]
	s_and_saveexec_b64 s[40:41], vcc
	s_cbranch_execz .LBB0_1567
	v_mov_b32_e32 v7, v2
	v_readlane_b32 s4, v254, 21
	v_readlane_b32 s5, v254, 22
	s_nop 4
	global_load_dword v2, v3, s[4:5] sc1
	s_mov_b64 s[4:5], 0
	s_waitcnt vmcnt(0)
	v_cmp_lt_u32_e32 vcc, v2, v7
	s_and_saveexec_b64 s[42:43], vcc
	s_cbranch_execz .LBB0_1566
	s_mov_b32 s17, 1
	s_branch .LBB0_1559

; __device__ __forceinline__ unsigned xb_ld(unsigned* p)              { return __hip_atomic_load(p, __ATOMIC_RELAXED, __HIP_MEMORY_SCOPE_AGENT); }
; __device__ __forceinline__ unsigned xb_add(unsigned* p, unsigned v) { return __hip_atomic_fetch_add(p, v, __ATOMIC_RELAXED, __HIP_MEMORY_SCOPE_AGENT); }
; #define XB_SPIN(cond, bar) do { unsigned _sp = 0; while (cond) { __builtin_amdgcn_s_sleep(1); \
;     if ((++_sp & 255u) == 0u) { if (xb_ld(&(bar)[XB_TMO])) break; if (_sp > XB_SPIN_CAP) { atomicAdd(&(bar)[XB_TMO], 1u); break; } } } } while (0)
; __device__ __forceinline__ void xcd_barrier(const XcdBarrier& b) {
;     ...
;         const unsigned old = xb_add(&bar[XB_XSUB(b.x)], 1u);
;         const unsigned gen = old / nloc;
;         if (old + 1u == (gen + 1u) * nloc) {
;             __builtin_amdgcn_fence(__ATOMIC_RELEASE, "agent");
;             asm volatile("s_waitcnt vmcnt(0)" ::: "memory");
;             const unsigned og = xb_add(&bar[XB_TOP], 1u);
;             const unsigned tg = og / nx;
;             if (og + 1u == (tg + 1u) * nx) xb_add(&bar[XB_TOPGEN], 1u);
;             else XB_SPIN(xb_ld(&bar[XB_TOPGEN]) == tg, bar);
;             __builtin_amdgcn_fence(__ATOMIC_ACQUIRE, "agent");
;             xb_add(&bar[XB_XGEN(b.x)], 1u);
;             asm volatile("s_waitcnt vmcnt(0)" ::: "memory");
;         } else {
;             XB_SPIN(xb_ld(&bar[XB_XGEN(b.x)]) == gen, bar);
.LBB0_1761:
	v_readlane_b32 s4, v254, 17
	v_readlane_b32 s5, v254, 18
	v_cvt_f32_u32_e32 v1, v4
	v_sub_u32_e32 v6, 0, v4
	v_rcp_iflag_f32_e32 v1, v1
	s_nop 1
	global_atomic_add v5, v3, v244, s[4:5] sc0
	v_mul_f32_e32 v1, 0x4f7ffffe, v1
	v_cvt_u32_f32_e32 v1, v1
	v_mul_lo_u32 v6, v6, v1
	v_mul_hi_u32 v6, v1, v6
	v_add_u32_e32 v1, v1, v6
	s_waitcnt vmcnt(0)
	v_mul_hi_u32 v1, v5, v1
	v_mul_lo_u32 v6, v1, v4
	v_sub_u32_e32 v6, v5, v6
	v_add_u32_e32 v7, 1, v1
	v_cmp_ge_u32_e32 vcc, v6, v4
	v_add_u32_e32 v5, 1, v5
	s_nop 0
	v_cndmask_b32_e32 v1, v1, v7, vcc
	v_sub_u32_e32 v7, v6, v4
	v_cndmask_b32_e32 v6, v6, v7, vcc
	v_add_u32_e32 v7, 1, v1
	v_cmp_ge_u32_e32 vcc, v6, v4
	s_nop 1
	v_cndmask_b32_e32 v1, v1, v7, vcc
	v_mul_lo_u32 v6, v4, v1
	v_add_u32_e32 v4, v6, v4
	v_cmp_ne_u32_e32 vcc, v5, v4
	s_and_saveexec_b64 s[4:5], vcc
	s_xor_b64 s[44:45], exec, s[4:5]
	s_cbranch_execz .LBB0_1792
	v_readlane_b32 s4, v254, 21
	v_readlane_b32 s5, v254, 22
	s_waitcnt lgkmcnt(0)
	v_mad_u32_u24 v7, v1, v2, v2
	s_nop 3
	global_load_dword v2, v3, s[4:5] sc1
	s_waitcnt vmcnt(0)
	v_cmp_lt_u32_e32 vcc, v2, v7
	s_and_saveexec_b64 s[46:47], vcc
	s_cbranch_execz .LBB0_1791
	s_mov_b32 s17, 1
	s_mov_b64 s[4:5], 0
	s_branch .LBB0_1765

; __device__ __forceinline__ unsigned xb_ld(unsigned* p)              { return __hip_atomic_load(p, __ATOMIC_RELAXED, __HIP_MEMORY_SCOPE_AGENT); }
; __device__ __forceinline__ unsigned xb_add(unsigned* p, unsigned v) { return __hip_atomic_fetch_add(p, v, __ATOMIC_RELAXED, __HIP_MEMORY_SCOPE_AGENT); }
; #define XB_SPIN(cond, bar) do { unsigned _sp = 0; while (cond) { __builtin_amdgcn_s_sleep(1); \
;     if ((++_sp & 255u) == 0u) { if (xb_ld(&(bar)[XB_TMO])) break; if (_sp > XB_SPIN_CAP) { atomicAdd(&(bar)[XB_TMO], 1u); break; } } } } while (0)
; __device__ __forceinline__ void xcd_barrier(const XcdBarrier& b) {
;     ...
;             const unsigned og = xb_add(&bar[XB_TOP], 1u);
;             const unsigned tg = og / nx;
;             if (og + 1u == (tg + 1u) * nx) xb_add(&bar[XB_TOPGEN], 1u);
;             else XB_SPIN(xb_ld(&bar[XB_TOPGEN]) == tg, bar);
.LBB0_1795:
	s_or_b64 exec, exec, s[6:7]
	s_waitcnt vmcnt(0)
	v_readfirstlane_b32 s4, v4
	v_sub_u32_e32 v5, 0, v2
	v_readlane_b32 s6, v254, 23
	v_add_u32_e32 v4, s4, v1
	v_cvt_f32_u32_e32 v1, v2
	v_readlane_b32 s7, v254, 24
	s_mov_b64 s[4:5], -1
	v_rcp_iflag_f32_e32 v1, v1
	s_nop 0
	v_mul_f32_e32 v1, 0x4f7ffffe, v1
	v_cvt_u32_f32_e32 v1, v1
	v_mul_lo_u32 v5, v5, v1
	v_mul_hi_u32 v5, v1, v5
	v_add_u32_e32 v1, v1, v5
	v_mul_hi_u32 v1, v4, v1
	v_mul_lo_u32 v5, v1, v2
	v_sub_u32_e32 v5, v4, v5
	v_cmp_ge_u32_e32 vcc, v5, v2
	v_add_u32_e32 v6, 1, v1
	v_add_u32_e32 v4, 1, v4
	v_cndmask_b32_e32 v1, v1, v6, vcc
	v_sub_u32_e32 v6, v5, v2
	v_cndmask_b32_e32 v5, v5, v6, vcc
	v_cmp_ge_u32_e32 vcc, v5, v2
	v_add_u32_e32 v5, 1, v1
	s_nop 0
	v_cndmask_b32_e32 v1, v1, v5, vcc
	v_mul_lo_u32 v5, v2, v1
	v_add_u32_e32 v2, v5, v2
	v_cmp_ne_u32_e32 vcc, v4, v2
	v_mov_b64_e32 v[4:5], s[6:7]
	s_and_saveexec_b64 s[44:45], vcc
	s_cbranch_execz .LBB0_1904
	v_mov_b32_e32 v7, v2
	v_readlane_b32 s4, v254, 21
	v_readlane_b32 s5, v254, 22
	s_nop 4
	global_load_dword v2, v3, s[4:5] sc1
	s_mov_b64 s[4:5], 0
	s_waitcnt vmcnt(0)
	v_cmp_lt_u32_e32 vcc, v2, v7
	s_and_saveexec_b64 s[46:47], vcc
	s_cbranch_execz .LBB0_1903
	s_mov_b32 s17, 1
	s_branch .LBB0_1799
